# phase D sigmoid part: previous and next row loads get their own destinations and go out with the first five loads
# speedup vs baseline: 1.2047x; 1.0047x over previous
.LBB0_631:
	s_sub_u32 s100, s18, 0x140
	s_cmp_lt_u32 s100, 32
	s_cselect_b32 s101, 0x2e0, 0
	s_sub_u32 s100, s18, 0x420
	s_cmp_lt_u32 s100, 32
	s_cselect_b32 s100, 0xfffffd20, 0
	s_add_i32 s100, s100, s101
	s_add_i32 s100, s100, s18
	s_mul_hi_i32 s6, s100, 0x78787879
	s_lshr_b32 s7, s6, 31
	s_ashr_i32 s36, s6, 8
	s_add_i32 s36, s36, s7
	s_mul_i32 s6, s36, 0x220
	s_sub_i32 s42, s100, s6
	s_ashr_i32 s68, s42, 2
	s_lshl_b32 s50, s68, 6
	s_add_i32 s6, s50, 0x7fffe000
	s_and_b32 s6, s6, 0x7fffff00
	s_add_i32 s28, s6, 0x2000
	s_and_b32 s51, s50, 0xfffff000
	s_cmpk_lt_i32 s68, 0x80
	s_cselect_b64 s[6:7], -1, 0
	s_and_b64 s[40:41], s[6:7], exec
	s_cselect_b32 s40, s75, 0xc0
	s_cselect_b32 s28, s51, s28
	s_lshl_b32 s41, s42, 4
	s_and_b32 s40, s40, s50
	s_and_b32 s41, s41, 48
	s_or_b32 s40, s40, s41
	s_mov_b32 s42, 0x1100000
	s_cmpk_lt_i32 s100, 0x220
	s_cbranch_scc1 .LBB0_637
	s_and_saveexec_b64 s[58:59], s[2:3]
	s_cbranch_execz .LBB0_634
	s_and_b64 s[6:7], s[6:7], exec
	v_add_u32_e32 v14, s40, v73
	s_movk_i32 s6, 0x1000
	v_add_u32_e32 v2, s28, v14
	v_mov_b64_e32 v[0:1], s[10:11]
	s_cselect_b32 s41, s6, 0x100
	v_mad_i64_i32 v[0:1], s[6:7], v2, s95, v[0:1]
	v_lshl_add_u64 v[8:9], v[28:29], 1, v[0:1]
	s_mov_b64 s[6:7], 0x1000
	v_lshl_add_u64 v[12:13], v[8:9], 0, s[6:7]
	v_add_co_u32_e32 v8, vcc, 0x1000, v8
	global_load_dwordx4 v[0:3], v[30:31], off offset:16
	global_load_dwordx4 v[16:19], v[30:31], off
	global_load_dwordx4 v[4:7], v[32:33], off offset:16
	global_load_dwordx4 v[20:23], v[32:33], off
	v_addc_co_u32_e32 v9, vcc, 0, v9, vcc
	global_load_dwordx4 v[8:11], v[8:9], off
	v_add_u32_e32 v15, 1, v14
	v_cmp_gt_i32_e32 vcc, s41, v15
	v_cmp_lt_i32_e64 s[6:7], 0, v14
	s_nop 1
	v_cndmask_b32_e32 v104, 0, v186, vcc
	v_cndmask_b32_e64 v119, 0, -1, s[6:7]
	v_cndmask_b32_e64 v118, 0, v185, s[6:7]
	v_lshl_add_u64 v[120:121], v[12:13], 0, v[104:105]
	v_lshl_add_u64 v[118:119], v[12:13], 0, v[118:119]
	global_load_dwordx4 v[110:113], v[118:119], off
	global_load_dwordx4 v[114:117], v[120:121], off
	s_waitcnt vmcnt(5)
	v_mov_b32_e32 v50, v16
	s_waitcnt vmcnt(3)
	v_mov_b32_e32 v51, v20
	v_mov_b32_e32 v20, v17
	s_waitcnt vmcnt(2)
	v_lshlrev_b32_e32 v42, 16, v8
	v_and_b32_e32 v44, 0xffff0000, v8
	v_lshlrev_b32_e32 v46, 16, v9
	v_and_b32_e32 v40, 0xffff0000, v9
	v_lshlrev_b32_e32 v38, 16, v10
	v_and_b32_e32 v36, 0xffff0000, v10
	v_lshlrev_b32_e32 v26, 16, v11
	v_and_b32_e32 v24, 0xffff0000, v11
	s_nop 0
	s_waitcnt vmcnt(1)
	v_lshlrev_b32_e32 v39, 16, v110
	v_cndmask_b32_e64 v48, 0, v39, s[6:7]
	s_waitcnt vmcnt(0)
	v_lshlrev_b32_e32 v41, 16, v114
	v_cndmask_b32_e32 v49, 0, v41, vcc
	v_pk_add_f32 v[48:49], v[48:49], v[42:43] op_sel_hi:[1,0] neg_lo:[0,1] neg_hi:[0,1]
	v_and_b32_e32 v12, 0xffff0000, v114
	v_pk_mul_f32 v[48:49], v[50:51], v[48:49]
	v_and_b32_e32 v8, 0xffff0000, v110
	v_add_f32_e32 v16, v48, v42
	v_cndmask_b32_e32 v43, 0, v12, vcc
	v_cndmask_b32_e64 v42, 0, v8, s[6:7]
	v_pk_add_f32 v[42:43], v[42:43], v[44:45] op_sel_hi:[1,0] neg_lo:[0,1] neg_hi:[0,1]
	v_lshlrev_b32_e32 v17, 16, v115
	v_pk_mul_f32 v[20:21], v[20:21], v[42:43]
	v_mov_b32_e32 v42, v18
	v_add_f32_e32 v8, v20, v44
	v_add_f32_e32 v8, v8, v21
	v_mul_f32_e32 v8, 0xbfb8aa3b, v8
	v_exp_f32_e32 v8, v8
	v_cndmask_b32_e32 v21, 0, v17, vcc
	v_mov_b32_e32 v43, v22
	v_mov_b32_e32 v22, v19
	v_add_f32_e32 v8, 1.0, v8
	v_rcp_f32_e32 v12, v8
	v_lshlrev_b32_e32 v8, 16, v111
	v_cndmask_b32_e64 v20, 0, v8, s[6:7]
	v_pk_add_f32 v[20:21], v[20:21], v[46:47] op_sel_hi:[1,0] neg_lo:[0,1] neg_hi:[0,1]
	v_mov_b32_e32 v18, v0
	v_pk_mul_f32 v[20:21], v[42:43], v[20:21]
	v_mov_b32_e32 v19, v4
	v_add_f32_e32 v8, v20, v46
	v_add_f32_e32 v8, v8, v21
	v_mul_f32_e32 v8, 0xbfb8aa3b, v8
	v_exp_f32_e32 v8, v8
	v_and_b32_e32 v4, 0xffff0000, v112
	v_and_b32_e32 v27, 0xffff0000, v113
	v_and_b32_e32 v25, 0xffff0000, v117
	v_add_f32_e32 v8, 1.0, v8
	v_rcp_f32_e32 v17, v8
	v_and_b32_e32 v8, 0xffff0000, v115
	v_and_b32_e32 v13, 0xffff0000, v111
	v_cndmask_b32_e32 v9, 0, v8, vcc
	v_cndmask_b32_e64 v8, 0, v13, s[6:7]
	v_pk_add_f32 v[8:9], v[8:9], v[40:41] op_sel_hi:[1,0] neg_lo:[0,1] neg_hi:[0,1]
	v_add_f32_e32 v16, v16, v49
	v_pk_mul_f32 v[8:9], v[22:23], v[8:9]
	v_mul_f32_e32 v16, 0xbfb8aa3b, v16
	v_add_f32_e32 v8, v8, v40
	v_add_f32_e32 v8, v8, v9
	v_mul_f32_e32 v8, 0xbfb8aa3b, v8
	v_exp_f32_e32 v8, v8
	v_lshlrev_b32_e32 v9, 16, v116
	v_cndmask_b32_e32 v9, 0, v9, vcc
	v_exp_f32_e32 v16, v16
	v_add_f32_e32 v8, 1.0, v8
	v_rcp_f32_e32 v13, v8
	v_lshlrev_b32_e32 v8, 16, v112
	v_cndmask_b32_e64 v8, 0, v8, s[6:7]
	v_pk_add_f32 v[8:9], v[8:9], v[38:39] op_sel_hi:[1,0] neg_lo:[0,1] neg_hi:[0,1]
	v_add_f32_e32 v16, 1.0, v16
	v_pk_mul_f32 v[8:9], v[18:19], v[8:9]
	v_rcp_f32_e32 v16, v16
	v_add_f32_e32 v0, v8, v38
	v_add_f32_e32 v0, v0, v9
	v_mul_f32_e32 v0, 0xbfb8aa3b, v0
	v_exp_f32_e32 v0, v0
	v_cndmask_b32_e64 v8, 0, v4, s[6:7]
	v_mov_b32_e32 v4, v1
	v_add_f32_e32 v0, 1.0, v0
	v_rcp_f32_e32 v18, v0
	v_and_b32_e32 v0, 0xffff0000, v116
	v_cndmask_b32_e32 v9, 0, v0, vcc
	v_pk_add_f32 v[8:9], v[8:9], v[36:37] op_sel_hi:[1,0] neg_lo:[0,1] neg_hi:[0,1]
	s_nop 0
	v_pk_mul_f32 v[0:1], v[4:5], v[8:9]
	v_mov_b32_e32 v4, v2
	v_add_f32_e32 v0, v0, v36
	v_add_f32_e32 v0, v0, v1
	v_mul_f32_e32 v0, 0xbfb8aa3b, v0
	v_exp_f32_e32 v0, v0
	v_lshlrev_b32_e32 v1, 16, v117
	v_cndmask_b32_e32 v1, 0, v1, vcc
	v_mov_b32_e32 v5, v6
	v_add_f32_e32 v0, 1.0, v0
	v_rcp_f32_e32 v8, v0
	v_lshlrev_b32_e32 v0, 16, v113
	v_cndmask_b32_e64 v0, 0, v0, s[6:7]
	v_pk_add_f32 v[0:1], v[0:1], v[26:27] op_sel_hi:[1,0] neg_lo:[0,1] neg_hi:[0,1]
	v_mov_b32_e32 v6, v3
	v_pk_mul_f32 v[0:1], v[4:5], v[0:1]
	v_cvt_pk_bf16_f32 v2, v18, v8
	v_add_f32_e32 v0, v0, v26
	v_add_f32_e32 v0, v0, v1
	v_mul_f32_e32 v0, 0xbfb8aa3b, v0
	v_exp_f32_e32 v0, v0
	v_cndmask_b32_e32 v1, 0, v25, vcc
	v_add_f32_e32 v0, 1.0, v0
	v_rcp_f32_e32 v4, v0
	v_cndmask_b32_e64 v0, 0, v27, s[6:7]
	v_pk_add_f32 v[0:1], v[0:1], v[24:25] op_sel_hi:[1,0] neg_lo:[0,1] neg_hi:[0,1]
	s_nop 0
	v_pk_mul_f32 v[0:1], v[6:7], v[0:1]
	s_nop 0
	v_add_f32_e32 v0, v0, v24
	v_add_f32_e32 v0, v0, v1
	v_mul_f32_e32 v0, 0xbfb8aa3b, v0
	v_exp_f32_e32 v0, v0
	v_cvt_pk_bf16_f32 v1, v17, v13
	v_add_f32_e32 v0, 1.0, v0
	v_rcp_f32_e32 v3, v0
	v_cvt_pk_bf16_f32 v0, v16, v12
	v_cvt_pk_bf16_f32 v3, v4, v3
	ds_write_b128 v74, v[0:3]
